# speedup vs baseline: 1.0038x; 1.0038x over previous
.Lgemm_peel:
	ds_read_b128 v[188:191], v1 offset:24576
	ds_read_b64 v[192:193], v172 offset:24640
	ds_read_b128 v[194:197], v1 offset:26112
	ds_read_b64 v[198:199], v172 offset:26176
	ds_read_b128 v[200:203], v170 offset:36864
	ds_read_b64 v[204:205], v173 offset:36928
	ds_read_b128 v[206:209], v170 offset:38400
	ds_read_b64 v[210:211], v173 offset:38464
	ds_read_b128 v[212:215], v170 offset:39936
	ds_read_b64 v[216:217], v173 offset:40000
	ds_read_b128 v[218:221], v170 offset:41472
	ds_read_b64 v[222:223], v173 offset:41536
	s_mov_b32 m0, s76
	s_add_u32 s38, s72, 0xffffa000
	s_addc_u32 s39, s73, -1
	v_mfma_scale_f32_16x16x128_f8f6f4 v[164:167], v[2:7], v[20:25], 0, v187, v187 op_sel_hi:[0,0,0] cbsz:2 blgp:2
	v_mfma_scale_f32_16x16x128_f8f6f4 v[160:163], v[8:13], v[20:25], 0, v187, v187 op_sel_hi:[0,0,0] cbsz:2 blgp:2
	v_mfma_scale_f32_16x16x128_f8f6f4 v[156:159], v[14:19], v[20:25], 0, v187, v187 op_sel_hi:[0,0,0] cbsz:2 blgp:2
	v_mfma_scale_f32_16x16x128_f8f6f4 v[152:155], v[26:31], v[20:25], 0, v187, v187 op_sel_hi:[0,0,0] cbsz:2 blgp:2
	v_mfma_scale_f32_16x16x128_f8f6f4 v[148:151], v[2:7], v[32:37], 0, v187, v187 op_sel_hi:[0,0,0] cbsz:2 blgp:2
	v_mfma_scale_f32_16x16x128_f8f6f4 v[140:143], v[8:13], v[32:37], 0, v187, v187 op_sel_hi:[0,0,0] cbsz:2 blgp:2
	v_mfma_scale_f32_16x16x128_f8f6f4 v[132:135], v[14:19], v[32:37], 0, v187, v187 op_sel_hi:[0,0,0] cbsz:2 blgp:2
	v_mfma_scale_f32_16x16x128_f8f6f4 v[124:127], v[26:31], v[32:37], 0, v187, v187 op_sel_hi:[0,0,0] cbsz:2 blgp:2
	s_cbranch_vccz .Lpst0_other
	s_waitcnt vmcnt(0)
	s_barrier
	global_load_lds_dwordx4 v228, s[38:39] offset:-3072
	global_load_lds_dwordx4 v228, s[38:39] offset:-2048
	global_load_lds_dwordx4 v228, s[38:39] offset:-1024
	global_load_lds_dwordx4 v228, s[38:39]
	global_load_lds_dwordx4 v228, s[38:39] offset:1024
	global_load_lds_dwordx4 v228, s[38:39] offset:2048
	s_branch .Lpst0_join

.Lpst0_join:
	s_waitcnt lgkmcnt(0)
	v_mfma_scale_f32_16x16x128_f8f6f4 v[112:115], v[2:7], v[188:193], 0, v187, v187 op_sel_hi:[0,0,0] cbsz:2 blgp:2
	v_mfma_scale_f32_16x16x128_f8f6f4 v[100:103], v[8:13], v[188:193], 0, v187, v187 op_sel_hi:[0,0,0] cbsz:2 blgp:2
	v_mfma_scale_f32_16x16x128_f8f6f4 v[92:95], v[14:19], v[188:193], 0, v187, v187 op_sel_hi:[0,0,0] cbsz:2 blgp:2
	v_mfma_scale_f32_16x16x128_f8f6f4 v[88:91], v[26:31], v[188:193], 0, v187, v187 op_sel_hi:[0,0,0] cbsz:2 blgp:2
	v_mfma_scale_f32_16x16x128_f8f6f4 v[84:87], v[2:7], v[194:199], 0, v187, v187 op_sel_hi:[0,0,0] cbsz:2 blgp:2
	v_mfma_scale_f32_16x16x128_f8f6f4 v[76:79], v[8:13], v[194:199], 0, v187, v187 op_sel_hi:[0,0,0] cbsz:2 blgp:2
	v_mfma_scale_f32_16x16x128_f8f6f4 v[68:71], v[14:19], v[194:199], 0, v187, v187 op_sel_hi:[0,0,0] cbsz:2 blgp:2
	v_mfma_scale_f32_16x16x128_f8f6f4 v[60:63], v[26:31], v[194:199], 0, v187, v187 op_sel_hi:[0,0,0] cbsz:2 blgp:2
	ds_read_b128 v[2:5], v170 offset:61440
	ds_read_b64 v[6:7], v173 offset:61504
	ds_read_b128 v[8:11], v170 offset:62976
	ds_read_b64 v[12:13], v173 offset:63040
	ds_read_b128 v[14:17], v170 offset:64512
	ds_read_b64 v[18:19], v173 offset:64576
	ds_read_b128 v[26:29], v171 offset:53760
	ds_read_b64 v[30:31], v174 offset:53760
	s_mov_b32 m0, s76
	s_add_u32 s38, s72, 0xffffd000
	s_addc_u32 s39, s73, -1
	v_mfma_scale_f32_16x16x128_f8f6f4 v[144:147], v[200:205], v[20:25], 0, v187, v187 op_sel_hi:[0,0,0] cbsz:2 blgp:2
	v_mfma_scale_f32_16x16x128_f8f6f4 v[136:139], v[206:211], v[20:25], 0, v187, v187 op_sel_hi:[0,0,0] cbsz:2 blgp:2
	v_mfma_scale_f32_16x16x128_f8f6f4 v[128:131], v[212:217], v[20:25], 0, v187, v187 op_sel_hi:[0,0,0] cbsz:2 blgp:2
	v_mfma_scale_f32_16x16x128_f8f6f4 v[120:123], v[218:223], v[20:25], 0, v187, v187 op_sel_hi:[0,0,0] cbsz:2 blgp:2
	v_mfma_scale_f32_16x16x128_f8f6f4 v[116:119], v[200:205], v[32:37], 0, v187, v187 op_sel_hi:[0,0,0] cbsz:2 blgp:2
	v_mfma_scale_f32_16x16x128_f8f6f4 v[108:111], v[206:211], v[32:37], 0, v187, v187 op_sel_hi:[0,0,0] cbsz:2 blgp:2
	v_mfma_scale_f32_16x16x128_f8f6f4 v[104:107], v[212:217], v[32:37], 0, v187, v187 op_sel_hi:[0,0,0] cbsz:2 blgp:2
	v_mfma_scale_f32_16x16x128_f8f6f4 v[96:99], v[218:223], v[32:37], 0, v187, v187 op_sel_hi:[0,0,0] cbsz:2 blgp:2
	ds_read_b128 v[20:23], v1 offset:49152
	ds_read_b64 v[24:25], v172 offset:49216
	ds_read_b128 v[32:35], v1 offset:50688
	ds_read_b64 v[36:37], v172 offset:50752
	s_cbranch_vccnz .Lpst1_other
	s_waitcnt vmcnt(0)
	s_barrier
	global_load_lds_dwordx4 v228, s[38:39] offset:-3072
	global_load_lds_dwordx4 v228, s[38:39] offset:-2048
	global_load_lds_dwordx4 v228, s[38:39] offset:-1024
	global_load_lds_dwordx4 v228, s[38:39]
	global_load_lds_dwordx4 v228, s[38:39] offset:1024
	global_load_lds_dwordx4 v228, s[38:39] offset:2048
	s_branch .Lpst1_join

.Lpst1_join:
	v_mfma_scale_f32_16x16x128_f8f6f4 v[80:83], v[200:205], v[188:193], 0, v187, v187 op_sel_hi:[0,0,0] cbsz:2 blgp:2
	v_mfma_scale_f32_16x16x128_f8f6f4 v[72:75], v[206:211], v[188:193], 0, v187, v187 op_sel_hi:[0,0,0] cbsz:2 blgp:2
	v_mfma_scale_f32_16x16x128_f8f6f4 v[64:67], v[212:217], v[188:193], 0, v187, v187 op_sel_hi:[0,0,0] cbsz:2 blgp:2
	v_mfma_scale_f32_16x16x128_f8f6f4 v[56:59], v[218:223], v[188:193], 0, v187, v187 op_sel_hi:[0,0,0] cbsz:2 blgp:2
	v_mfma_scale_f32_16x16x128_f8f6f4 v[52:55], v[200:205], v[194:199], 0, v187, v187 op_sel_hi:[0,0,0] cbsz:2 blgp:2
	v_mfma_scale_f32_16x16x128_f8f6f4 v[224:227], v[206:211], v[194:199], 0, v187, v187 op_sel_hi:[0,0,0] cbsz:2 blgp:2
	v_mfma_scale_f32_16x16x128_f8f6f4 v[212:215], v[212:217], v[194:199], 0, v187, v187 op_sel_hi:[0,0,0] cbsz:2 blgp:2
	v_mfma_scale_f32_16x16x128_f8f6f4 v[216:219], v[218:223], v[194:199], 0, v187, v187 op_sel_hi:[0,0,0] cbsz:2 blgp:2
	s_waitcnt lgkmcnt(0)
	s_nop 0
	ds_read_b128 v[40:43], v175
	ds_read_b64 v[44:45], v176
	ds_read_b128 v[188:191], v179
	ds_read_b64 v[192:193], v180
	ds_read_b128 v[46:49], v177
	ds_read_b64 v[50:51], v178
	ds_read_b128 v[194:197], v181
	ds_read_b64 v[198:199], v182
	ds_read_b128 v[200:203], v183
	ds_read_b64 v[204:205], v184
	ds_read_b128 v[206:209], v185
	ds_read_b64 v[210:211], v186
	s_mov_b32 m0, s77
	s_mov_b64 s[38:39], s[72:73]
	v_mfma_scale_f32_16x16x128_f8f6f4 v[164:167], v[2:7], v[20:25], v[164:167], v187, v187 op_sel_hi:[0,0,0] cbsz:2 blgp:2
	v_mfma_scale_f32_16x16x128_f8f6f4 v[160:163], v[8:13], v[20:25], v[160:163], v187, v187 op_sel_hi:[0,0,0] cbsz:2 blgp:2
	v_mfma_scale_f32_16x16x128_f8f6f4 v[156:159], v[14:19], v[20:25], v[156:159], v187, v187 op_sel_hi:[0,0,0] cbsz:2 blgp:2
	v_mfma_scale_f32_16x16x128_f8f6f4 v[152:155], v[26:31], v[20:25], v[152:155], v187, v187 op_sel_hi:[0,0,0] cbsz:2 blgp:2
	v_mfma_scale_f32_16x16x128_f8f6f4 v[148:151], v[2:7], v[32:37], v[148:151], v187, v187 op_sel_hi:[0,0,0] cbsz:2 blgp:2
	v_mfma_scale_f32_16x16x128_f8f6f4 v[140:143], v[8:13], v[32:37], v[140:143], v187, v187 op_sel_hi:[0,0,0] cbsz:2 blgp:2
	v_mfma_scale_f32_16x16x128_f8f6f4 v[132:135], v[14:19], v[32:37], v[132:135], v187, v187 op_sel_hi:[0,0,0] cbsz:2 blgp:2
	v_mfma_scale_f32_16x16x128_f8f6f4 v[124:127], v[26:31], v[32:37], v[124:127], v187, v187 op_sel_hi:[0,0,0] cbsz:2 blgp:2
	s_cbranch_vccz .Lpst2_other
	s_waitcnt vmcnt(0)
	s_barrier
	global_load_lds_dwordx4 v228, s[38:39] offset:-3072
	global_load_lds_dwordx4 v228, s[38:39] offset:-2048
	global_load_lds_dwordx4 v228, s[38:39] offset:-1024
	global_load_lds_dwordx4 v228, s[38:39]
	global_load_lds_dwordx4 v228, s[38:39] offset:1024
	global_load_lds_dwordx4 v228, s[38:39] offset:2048
	s_branch .Lpst2_join

.Lpst2_join:
	s_waitcnt lgkmcnt(0)
	v_mfma_scale_f32_16x16x128_f8f6f4 v[112:115], v[2:7], v[40:45], v[112:115], v187, v187 op_sel_hi:[0,0,0] cbsz:2 blgp:2
	v_mfma_scale_f32_16x16x128_f8f6f4 v[100:103], v[8:13], v[40:45], v[100:103], v187, v187 op_sel_hi:[0,0,0] cbsz:2 blgp:2
	v_mfma_scale_f32_16x16x128_f8f6f4 v[92:95], v[14:19], v[40:45], v[92:95], v187, v187 op_sel_hi:[0,0,0] cbsz:2 blgp:2
	v_mfma_scale_f32_16x16x128_f8f6f4 v[88:91], v[26:31], v[40:45], v[88:91], v187, v187 op_sel_hi:[0,0,0] cbsz:2 blgp:2
	v_mfma_scale_f32_16x16x128_f8f6f4 v[84:87], v[2:7], v[188:193], v[84:87], v187, v187 op_sel_hi:[0,0,0] cbsz:2 blgp:2
	v_mfma_scale_f32_16x16x128_f8f6f4 v[76:79], v[8:13], v[188:193], v[76:79], v187, v187 op_sel_hi:[0,0,0] cbsz:2 blgp:2
	v_mfma_scale_f32_16x16x128_f8f6f4 v[68:71], v[14:19], v[188:193], v[68:71], v187, v187 op_sel_hi:[0,0,0] cbsz:2 blgp:2
	v_mfma_scale_f32_16x16x128_f8f6f4 v[60:63], v[26:31], v[188:193], v[60:63], v187, v187 op_sel_hi:[0,0,0] cbsz:2 blgp:2
	ds_read_b128 v[2:5], v170 offset:12288
	ds_read_b64 v[6:7], v173 offset:12352
	ds_read_b128 v[8:11], v170 offset:13824
	ds_read_b64 v[12:13], v173 offset:13888
	ds_read_b128 v[14:17], v170 offset:15360
	ds_read_b64 v[18:19], v173 offset:15424
	ds_read_b128 v[26:29], v170 offset:16896
	ds_read_b64 v[30:31], v173 offset:16960
	s_mov_b32 m0, s77
	s_add_u32 s38, s72, 0x3000
	s_addc_u32 s39, s73, 0
	v_mfma_scale_f32_16x16x128_f8f6f4 v[144:147], v[46:51], v[20:25], v[144:147], v187, v187 op_sel_hi:[0,0,0] cbsz:2 blgp:2
	v_mfma_scale_f32_16x16x128_f8f6f4 v[136:139], v[194:199], v[20:25], v[136:139], v187, v187 op_sel_hi:[0,0,0] cbsz:2 blgp:2
	v_mfma_scale_f32_16x16x128_f8f6f4 v[128:131], v[200:205], v[20:25], v[128:131], v187, v187 op_sel_hi:[0,0,0] cbsz:2 blgp:2
	v_mfma_scale_f32_16x16x128_f8f6f4 v[120:123], v[206:211], v[20:25], v[120:123], v187, v187 op_sel_hi:[0,0,0] cbsz:2 blgp:2
	v_mfma_scale_f32_16x16x128_f8f6f4 v[116:119], v[46:51], v[32:37], v[116:119], v187, v187 op_sel_hi:[0,0,0] cbsz:2 blgp:2
	v_mfma_scale_f32_16x16x128_f8f6f4 v[108:111], v[194:199], v[32:37], v[108:111], v187, v187 op_sel_hi:[0,0,0] cbsz:2 blgp:2
	v_mfma_scale_f32_16x16x128_f8f6f4 v[104:107], v[200:205], v[32:37], v[104:107], v187, v187 op_sel_hi:[0,0,0] cbsz:2 blgp:2
	v_mfma_scale_f32_16x16x128_f8f6f4 v[96:99], v[206:211], v[32:37], v[96:99], v187, v187 op_sel_hi:[0,0,0] cbsz:2 blgp:2
	ds_read_b128 v[20:23], v1
	ds_read_b64 v[24:25], v172 offset:64
	ds_read_b128 v[32:35], v1 offset:1536
	ds_read_b64 v[36:37], v172 offset:1600
	s_cbranch_vccnz .Lpst3_other
	s_waitcnt vmcnt(0)
	s_barrier
	global_load_lds_dwordx4 v228, s[38:39] offset:-3072
	global_load_lds_dwordx4 v228, s[38:39] offset:-2048
	global_load_lds_dwordx4 v228, s[38:39] offset:-1024
	global_load_lds_dwordx4 v228, s[38:39]
	global_load_lds_dwordx4 v228, s[38:39] offset:1024
	global_load_lds_dwordx4 v228, s[38:39] offset:2048
	s_branch .Lpst3_join

.LBB1_3:
	ds_read_b128 v[188:191], v1 offset:24576
	ds_read_b64 v[192:193], v172 offset:24640
	ds_read_b128 v[194:197], v1 offset:26112
	ds_read_b64 v[198:199], v172 offset:26176
	ds_read_b128 v[200:203], v170 offset:36864
	ds_read_b64 v[204:205], v173 offset:36928
	ds_read_b128 v[206:209], v170 offset:38400
	ds_read_b64 v[210:211], v173 offset:38464
	ds_read_b128 v[212:215], v170 offset:39936
	ds_read_b64 v[216:217], v173 offset:40000
	ds_read_b128 v[218:221], v170 offset:41472
	ds_read_b64 v[222:223], v173 offset:41536
	s_mov_b32 m0, s76
	s_add_u32 s38, s72, 0xffffa000
	s_addc_u32 s39, s73, -1
	v_mfma_scale_f32_16x16x128_f8f6f4 v[164:167], v[2:7], v[20:25], v[164:167], v187, v187 op_sel_hi:[0,0,0] cbsz:2 blgp:2
	v_mfma_scale_f32_16x16x128_f8f6f4 v[160:163], v[8:13], v[20:25], v[160:163], v187, v187 op_sel_hi:[0,0,0] cbsz:2 blgp:2
	v_mfma_scale_f32_16x16x128_f8f6f4 v[156:159], v[14:19], v[20:25], v[156:159], v187, v187 op_sel_hi:[0,0,0] cbsz:2 blgp:2
	v_mfma_scale_f32_16x16x128_f8f6f4 v[152:155], v[26:31], v[20:25], v[152:155], v187, v187 op_sel_hi:[0,0,0] cbsz:2 blgp:2
	v_mfma_scale_f32_16x16x128_f8f6f4 v[148:151], v[2:7], v[32:37], v[148:151], v187, v187 op_sel_hi:[0,0,0] cbsz:2 blgp:2
	v_mfma_scale_f32_16x16x128_f8f6f4 v[140:143], v[8:13], v[32:37], v[140:143], v187, v187 op_sel_hi:[0,0,0] cbsz:2 blgp:2
	v_mfma_scale_f32_16x16x128_f8f6f4 v[132:135], v[14:19], v[32:37], v[132:135], v187, v187 op_sel_hi:[0,0,0] cbsz:2 blgp:2
	v_mfma_scale_f32_16x16x128_f8f6f4 v[124:127], v[26:31], v[32:37], v[124:127], v187, v187 op_sel_hi:[0,0,0] cbsz:2 blgp:2
	s_cbranch_vccz .Lst0_other
	s_waitcnt vmcnt(0)
	s_barrier
	global_load_lds_dwordx4 v228, s[38:39] offset:-3072
	global_load_lds_dwordx4 v228, s[38:39] offset:-2048
	global_load_lds_dwordx4 v228, s[38:39] offset:-1024
	global_load_lds_dwordx4 v228, s[38:39]
	global_load_lds_dwordx4 v228, s[38:39] offset:1024
	global_load_lds_dwordx4 v228, s[38:39] offset:2048
	s_branch .Lst0_join

.Lst0_join:
	s_waitcnt lgkmcnt(0)
	v_mfma_scale_f32_16x16x128_f8f6f4 v[112:115], v[2:7], v[188:193], v[112:115], v187, v187 op_sel_hi:[0,0,0] cbsz:2 blgp:2
	v_mfma_scale_f32_16x16x128_f8f6f4 v[100:103], v[8:13], v[188:193], v[100:103], v187, v187 op_sel_hi:[0,0,0] cbsz:2 blgp:2
	v_mfma_scale_f32_16x16x128_f8f6f4 v[92:95], v[14:19], v[188:193], v[92:95], v187, v187 op_sel_hi:[0,0,0] cbsz:2 blgp:2
	v_mfma_scale_f32_16x16x128_f8f6f4 v[88:91], v[26:31], v[188:193], v[88:91], v187, v187 op_sel_hi:[0,0,0] cbsz:2 blgp:2
	v_mfma_scale_f32_16x16x128_f8f6f4 v[84:87], v[2:7], v[194:199], v[84:87], v187, v187 op_sel_hi:[0,0,0] cbsz:2 blgp:2
	v_mfma_scale_f32_16x16x128_f8f6f4 v[76:79], v[8:13], v[194:199], v[76:79], v187, v187 op_sel_hi:[0,0,0] cbsz:2 blgp:2
	v_mfma_scale_f32_16x16x128_f8f6f4 v[68:71], v[14:19], v[194:199], v[68:71], v187, v187 op_sel_hi:[0,0,0] cbsz:2 blgp:2
	v_mfma_scale_f32_16x16x128_f8f6f4 v[60:63], v[26:31], v[194:199], v[60:63], v187, v187 op_sel_hi:[0,0,0] cbsz:2 blgp:2
	ds_read_b128 v[2:5], v170 offset:61440
	ds_read_b64 v[6:7], v173 offset:61504
	ds_read_b128 v[8:11], v170 offset:62976
	ds_read_b64 v[12:13], v173 offset:63040
	ds_read_b128 v[14:17], v170 offset:64512
	ds_read_b64 v[18:19], v173 offset:64576
	ds_read_b128 v[26:29], v171 offset:53760
	ds_read_b64 v[30:31], v174 offset:53760
	s_mov_b32 m0, s76
	s_add_u32 s38, s72, 0xffffd000
	s_addc_u32 s39, s73, -1
	v_mfma_scale_f32_16x16x128_f8f6f4 v[144:147], v[200:205], v[20:25], v[144:147], v187, v187 op_sel_hi:[0,0,0] cbsz:2 blgp:2
	v_mfma_scale_f32_16x16x128_f8f6f4 v[136:139], v[206:211], v[20:25], v[136:139], v187, v187 op_sel_hi:[0,0,0] cbsz:2 blgp:2
	v_mfma_scale_f32_16x16x128_f8f6f4 v[128:131], v[212:217], v[20:25], v[128:131], v187, v187 op_sel_hi:[0,0,0] cbsz:2 blgp:2
	v_mfma_scale_f32_16x16x128_f8f6f4 v[120:123], v[218:223], v[20:25], v[120:123], v187, v187 op_sel_hi:[0,0,0] cbsz:2 blgp:2
	v_mfma_scale_f32_16x16x128_f8f6f4 v[116:119], v[200:205], v[32:37], v[116:119], v187, v187 op_sel_hi:[0,0,0] cbsz:2 blgp:2
	v_mfma_scale_f32_16x16x128_f8f6f4 v[108:111], v[206:211], v[32:37], v[108:111], v187, v187 op_sel_hi:[0,0,0] cbsz:2 blgp:2
	v_mfma_scale_f32_16x16x128_f8f6f4 v[104:107], v[212:217], v[32:37], v[104:107], v187, v187 op_sel_hi:[0,0,0] cbsz:2 blgp:2
	v_mfma_scale_f32_16x16x128_f8f6f4 v[96:99], v[218:223], v[32:37], v[96:99], v187, v187 op_sel_hi:[0,0,0] cbsz:2 blgp:2
	ds_read_b128 v[20:23], v1 offset:49152
	ds_read_b64 v[24:25], v172 offset:49216
	ds_read_b128 v[32:35], v1 offset:50688
	ds_read_b64 v[36:37], v172 offset:50752
	s_cbranch_vccnz .Lst1_other
	s_waitcnt vmcnt(0)
	s_barrier
	global_load_lds_dwordx4 v228, s[38:39] offset:-3072
	global_load_lds_dwordx4 v228, s[38:39] offset:-2048
	global_load_lds_dwordx4 v228, s[38:39] offset:-1024
	global_load_lds_dwordx4 v228, s[38:39]
	global_load_lds_dwordx4 v228, s[38:39] offset:1024
	global_load_lds_dwordx4 v228, s[38:39] offset:2048
	s_branch .Lst1_join

.Lst1_join:
	v_mfma_scale_f32_16x16x128_f8f6f4 v[80:83], v[200:205], v[188:193], v[80:83], v187, v187 op_sel_hi:[0,0,0] cbsz:2 blgp:2
	v_mfma_scale_f32_16x16x128_f8f6f4 v[72:75], v[206:211], v[188:193], v[72:75], v187, v187 op_sel_hi:[0,0,0] cbsz:2 blgp:2
	v_mfma_scale_f32_16x16x128_f8f6f4 v[64:67], v[212:217], v[188:193], v[64:67], v187, v187 op_sel_hi:[0,0,0] cbsz:2 blgp:2
	v_mfma_scale_f32_16x16x128_f8f6f4 v[56:59], v[218:223], v[188:193], v[56:59], v187, v187 op_sel_hi:[0,0,0] cbsz:2 blgp:2
	v_mfma_scale_f32_16x16x128_f8f6f4 v[52:55], v[200:205], v[194:199], v[52:55], v187, v187 op_sel_hi:[0,0,0] cbsz:2 blgp:2
	v_mfma_scale_f32_16x16x128_f8f6f4 v[224:227], v[206:211], v[194:199], v[48:51], v187, v187 op_sel_hi:[0,0,0] cbsz:2 blgp:2
	v_mfma_scale_f32_16x16x128_f8f6f4 v[212:215], v[212:217], v[194:199], v[44:47], v187, v187 op_sel_hi:[0,0,0] cbsz:2 blgp:2
	v_mfma_scale_f32_16x16x128_f8f6f4 v[216:219], v[218:223], v[194:199], v[40:43], v187, v187 op_sel_hi:[0,0,0] cbsz:2 blgp:2
	s_waitcnt lgkmcnt(0)
	s_nop 0
	ds_read_b128 v[40:43], v175
	ds_read_b64 v[44:45], v176
	ds_read_b128 v[188:191], v179
	ds_read_b64 v[192:193], v180
	ds_read_b128 v[46:49], v177
	ds_read_b64 v[50:51], v178
	ds_read_b128 v[194:197], v181
	ds_read_b64 v[198:199], v182
	ds_read_b128 v[200:203], v183
	ds_read_b64 v[204:205], v184
	ds_read_b128 v[206:209], v185
	ds_read_b64 v[210:211], v186
	s_mov_b32 m0, s77
	s_mov_b64 s[38:39], s[72:73]
	v_mfma_scale_f32_16x16x128_f8f6f4 v[164:167], v[2:7], v[20:25], v[164:167], v187, v187 op_sel_hi:[0,0,0] cbsz:2 blgp:2
	v_mfma_scale_f32_16x16x128_f8f6f4 v[160:163], v[8:13], v[20:25], v[160:163], v187, v187 op_sel_hi:[0,0,0] cbsz:2 blgp:2
	v_mfma_scale_f32_16x16x128_f8f6f4 v[156:159], v[14:19], v[20:25], v[156:159], v187, v187 op_sel_hi:[0,0,0] cbsz:2 blgp:2
	v_mfma_scale_f32_16x16x128_f8f6f4 v[152:155], v[26:31], v[20:25], v[152:155], v187, v187 op_sel_hi:[0,0,0] cbsz:2 blgp:2
	v_mfma_scale_f32_16x16x128_f8f6f4 v[148:151], v[2:7], v[32:37], v[148:151], v187, v187 op_sel_hi:[0,0,0] cbsz:2 blgp:2
	v_mfma_scale_f32_16x16x128_f8f6f4 v[140:143], v[8:13], v[32:37], v[140:143], v187, v187 op_sel_hi:[0,0,0] cbsz:2 blgp:2
	v_mfma_scale_f32_16x16x128_f8f6f4 v[132:135], v[14:19], v[32:37], v[132:135], v187, v187 op_sel_hi:[0,0,0] cbsz:2 blgp:2
	v_mfma_scale_f32_16x16x128_f8f6f4 v[124:127], v[26:31], v[32:37], v[124:127], v187, v187 op_sel_hi:[0,0,0] cbsz:2 blgp:2
	s_cbranch_vccz .Lst2_other
	s_waitcnt vmcnt(0)
	s_barrier
	global_load_lds_dwordx4 v228, s[38:39] offset:-3072
	global_load_lds_dwordx4 v228, s[38:39] offset:-2048
	global_load_lds_dwordx4 v228, s[38:39] offset:-1024
	global_load_lds_dwordx4 v228, s[38:39]
	global_load_lds_dwordx4 v228, s[38:39] offset:1024
	global_load_lds_dwordx4 v228, s[38:39] offset:2048
	s_branch .Lst2_join
